# baseline (speedup 1.0000x reference)
.LBB2_13:
	v_exp_f32_e32 v48, v48
	v_exp_f32_e32 v49, v49
	v_mfma_f32_32x32x16_bf16 v[112:127], a[192:195], a[128:131], v[16:31]
	ds_read_b64_tr_b16 v[180:181], v223 offset:0
	v_cvt_pk_bf16_f32 v164, v128, v129
	v_exp_f32_e32 v50, v50
	v_exp_f32_e32 v51, v51
	v_mfma_f32_32x32x16_bf16 v[96:111], a[192:195], a[160:163], v[0:15]
	ds_read_b64_tr_b16 v[182:183], v223 offset:0x800
	v_cvt_pk_bf16_f32 v165, v130, v131
	v_mfma_f32_32x32x16_bf16 v[80:95], a[224:227], a[128:131], v[16:31]
	ds_read_b64_tr_b16 v[184:185], v223 offset:0x200
	v_exp_f32_e32 v236, v52
	v_exp_f32_e32 v237, v53
	v_cvt_pk_bf16_f32 v166, v132, v133
	v_mfma_f32_32x32x16_bf16 v[64:79], a[224:227], a[160:163], v[0:15]
	ds_read_b64_tr_b16 v[186:187], v223 offset:0xa00
	ds_read_b64_tr_b16 v[176:177], v223 offset:0x400
	v_exp_f32_e32 v242, v54
	v_exp_f32_e32 v243, v55
	v_cvt_pk_bf16_f32 v167, v134, v135
	v_exp_f32_e32 v198, v56
	v_exp_f32_e32 v199, v57
	v_mfma_f32_32x32x16_bf16 v[112:127], a[196:199], a[132:135], v[112:127]
	ds_read_b64_tr_b16 v[178:179], v223 offset:0xc00
	v_cvt_pk_bf16_f32 v128, v136, v137
	v_exp_f32_e32 v230, v58
	v_exp_f32_e32 v231, v59
	v_mfma_f32_32x32x16_bf16 v[96:111], a[196:199], a[164:167], v[96:111]
	ds_read_b64_tr_b16 v[188:189], v223 offset:0x600
	v_cvt_pk_bf16_f32 v129, v138, v139
	v_exp_f32_e32 v232, v60
	v_exp_f32_e32 v233, v61
	v_mfma_f32_32x32x16_bf16 v[80:95], a[228:231], a[132:135], v[80:95]
	ds_read_b64_tr_b16 v[190:191], v223 offset:0xe00
	v_cvt_pk_bf16_f32 v130, v140, v141
	v_mfma_f32_32x32x16_bf16 v[64:79], a[228:231], a[164:167], v[64:79]
	ds_read_b64_tr_b16 v[172:173], v223 offset:0x1000
	v_exp_f32_e32 v234, v62
	v_exp_f32_e32 v235, v63
	ds_read_b64_tr_b16 v[174:175], v223 offset:0x1800
	v_cvt_pk_bf16_f32 v131, v142, v143
	v_exp_f32_e32 v141, v32
	v_exp_f32_e32 v142, v33
	v_mfma_f32_32x32x16_bf16 v[112:127], a[200:203], a[136:139], v[112:127]
	ds_read_b64_tr_b16 v[168:169], v223 offset:0x1200
	v_cvt_pk_bf16_f32 v192, v144, v145
	v_exp_f32_e32 v143, v34
	v_mfma_f32_32x32x16_bf16 v[96:111], a[200:203], a[168:171], v[96:111]
	ds_read_b64_tr_b16 v[170:171], v223 offset:0x1a00
	v_exp_f32_e32 v244, v35
	v_cvt_pk_bf16_f32 v193, v146, v147
	v_mfma_f32_32x32x16_bf16 v[80:95], a[232:235], a[136:139], v[80:95]
	ds_read_b64_tr_b16 v[160:161], v223 offset:0x1400
	v_exp_f32_e32 v245, v36
	v_exp_f32_e32 v246, v37
	v_cvt_pk_bf16_f32 v194, v148, v149
	v_mfma_f32_32x32x16_bf16 v[64:79], a[232:235], a[168:171], v[64:79]
	ds_read_b64_tr_b16 v[162:163], v223 offset:0x1c00
	ds_read_b64_tr_b16 v[136:137], v223 offset:0x1600
	v_exp_f32_e32 v247, v38
	v_exp_f32_e32 v248, v39
	v_cvt_pk_bf16_f32 v195, v150, v151
	v_exp_f32_e32 v148, v40
	v_exp_f32_e32 v149, v41
	v_mfma_f32_32x32x16_bf16 v[112:127], a[204:207], a[140:143], v[112:127]
	ds_read_b64_tr_b16 v[138:139], v223 offset:0x1e00
	v_cvt_pk_bf16_f32 v144, v152, v153
	v_exp_f32_e32 v150, v42
	v_exp_f32_e32 v151, v43
	v_mfma_f32_32x32x16_bf16 v[96:111], a[204:207], a[172:175], v[96:111]
	ds_read_b64_tr_b16 v[132:133], v223 offset:0x2000
	v_cvt_pk_bf16_f32 v145, v154, v155
	v_exp_f32_e32 v152, v44
	v_exp_f32_e32 v153, v45
	v_mfma_f32_32x32x16_bf16 v[80:95], a[236:239], a[140:143], v[80:95]
	ds_read_b64_tr_b16 v[134:135], v223 offset:0x2800
	v_cvt_pk_bf16_f32 v146, v156, v157
	v_mfma_f32_32x32x16_bf16 v[64:79], a[236:239], a[172:175], v[64:79]
	ds_read_b64_tr_b16 v[60:61], v223 offset:0x2200
	v_exp_f32_e32 v154, v46
	v_exp_f32_e32 v155, v47
	ds_read_b64_tr_b16 v[62:63], v223 offset:0x2a00
	v_cvt_pk_bf16_f32 v147, v158, v159
	s_mov_b32 s0, s30
	v_mfma_f32_32x32x16_bf16 v[112:127], a[208:211], a[144:147], v[112:127]
	ds_read_b64_tr_b16 v[56:57], v223 offset:0x2400
	v_cvt_pk_bf16_f32 v52, v48, v49
	v_add_f32_e32 v32, v239, v48
	v_add_f32_e32 v33, v238, v49
	s_add_i32 s19, s17, 0xfffda000
	s_mov_b32 s1, s19
	v_mfma_f32_32x32x16_bf16 v[96:111], a[208:211], a[176:179], v[96:111]
	ds_read_b64_tr_b16 v[58:59], v223 offset:0x2c00
	v_cvt_pk_bf16_f32 v53, v50, v51
	v_add_f32_e32 v32, v32, v50
	v_add_f32_e32 v33, v33, v51
	s_mov_b32 s81, s37
	v_mfma_f32_32x32x16_bf16 v[80:95], a[240:243], a[144:147], v[80:95]
	ds_read_b64_tr_b16 v[48:49], v223 offset:0x2600
	v_cvt_pk_bf16_f32 v54, v236, v237
	v_add_f32_e32 v32, v32, v236
	v_add_f32_e32 v33, v33, v237
	s_add_i32 s82, s17, 0xfffdc000
	v_mfma_f32_32x32x16_bf16 v[64:79], a[240:243], a[176:179], v[64:79]
	ds_read_b64_tr_b16 v[50:51], v223 offset:0x2e00
	ds_read_b64_tr_b16 v[44:45], v223 offset:0x3000
	v_cvt_pk_bf16_f32 v55, v242, v243
	v_add_f32_e32 v32, v32, v242
	v_add_f32_e32 v33, v33, v243
	s_mov_b32 s83, s39
	v_mfma_f32_32x32x16_bf16 v[112:127], a[212:215], a[148:151], v[112:127]
	ds_read_b64_tr_b16 v[46:47], v223 offset:0x3800
	v_add_f32_e32 v32, v32, v198
	v_add_f32_e32 v33, v33, v199
	s_add_i32 s24, s17, 0xfffde000
	s_mov_b32 s84, s24
	v_mfma_f32_32x32x16_bf16 v[96:111], a[212:215], a[180:183], v[96:111]
	ds_read_b64_tr_b16 v[40:41], v223 offset:0x3200
	v_add_f32_e32 v32, v32, v230
	v_add_f32_e32 v33, v33, v231
	s_mov_b32 s85, s41
	v_mfma_f32_32x32x16_bf16 v[80:95], a[244:247], a[148:151], v[80:95]
	ds_read_b64_tr_b16 v[42:43], v223 offset:0x3a00
	v_add_f32_e32 v32, v32, v232
	v_add_f32_e32 v33, v33, v233
	s_add_i32 s86, s17, 0xfffe0000
	v_mfma_f32_32x32x16_bf16 v[64:79], a[244:247], a[180:183], v[64:79]
	ds_read_b64_tr_b16 v[36:37], v223 offset:0x3400
	ds_read_b64_tr_b16 v[38:39], v223 offset:0x3c00
	v_add_f32_e32 v156, v32, v234
	v_add_f32_e32 v157, v33, v235
	s_mov_b32 s87, s43
	v_mfma_f32_32x32x16_bf16 v[112:127], a[216:219], a[152:155], v[112:127]
	ds_read_b64_tr_b16 v[32:33], v223 offset:0x3600
	v_cvt_pk_bf16_f32 v140, v141, v142
	v_add_f32_e32 v158, v240, v141
	v_add_f32_e32 v142, v241, v142
	s_add_i32 s88, s17, 0xfffba000
	v_mfma_f32_32x32x16_bf16 v[96:111], a[216:219], a[184:187], v[96:111]
	ds_read_b64_tr_b16 v[34:35], v223 offset:0x3e00
	v_cvt_pk_bf16_f32 v141, v143, v244
	v_add_f32_e32 v143, v158, v143
	v_add_f32_e32 v158, v142, v244
	v_mfma_f32_32x32x16_bf16 v[80:95], a[248:251], a[152:155], v[80:95]
	s_mov_b32 s89, s45
	v_cvt_pk_bf16_f32 v142, v245, v246
	v_add_f32_e32 v159, v143, v245
	v_add_f32_e32 v158, v158, v246
	v_mfma_f32_32x32x16_bf16 v[64:79], a[248:251], a[184:187], v[64:79]
	s_add_i32 s90, s17, 0xfffba080
	v_cvt_pk_bf16_f32 v143, v247, v248
	v_add_f32_e32 v159, v159, v247
	v_add_f32_e32 v158, v158, v248
	v_mfma_f32_32x32x16_bf16 v[112:127], a[220:223], a[156:159], v[112:127]
	s_mov_b32 s91, s47
	v_add_f32_e32 v159, v159, v148
	v_add_f32_e32 v158, v158, v149
	v_mfma_f32_32x32x16_bf16 v[96:111], a[220:223], a[188:191], v[96:111]
	s_add_i32 s92, s17, 0xfffbe000
	v_add_f32_e32 v159, v159, v150
	v_add_f32_e32 v158, v158, v151
	v_mfma_f32_32x32x16_bf16 v[80:95], a[252:255], a[156:159], v[80:95]
	s_mov_b32 s93, s49
	v_add_f32_e32 v159, v159, v152
	v_add_f32_e32 v158, v158, v153
	v_mfma_f32_32x32x16_bf16 v[64:79], a[252:255], a[188:191], v[64:79]
	s_add_i32 s94, s17, 0xfffbe080
	v_add_f32_e32 v159, v159, v154
	v_add_f32_e32 v158, v158, v155
	v_add_f32_e32 v156, v156, v157
	s_waitcnt vmcnt(0) lgkmcnt(0)
	s_barrier
	v_add_f32_e32 v158, v159, v158
	v_mov_b32_e32 v157, v156
	v_mov_b32_e32 v159, v158
	s_nop 0
	v_permlane32_swap_b32_e32 v156, v157
	v_permlane32_swap_b32_e32 v158, v159
	v_add_f32_e32 v156, v156, v157
	v_add_f32_e32 v158, v158, v159
	v_add_f32_e32 v197, v197, v156
	v_add_f32_e32 v196, v196, v158
	s_mov_b32 m0, s0
	v_mfma_f32_32x32x16_bf16 a[0:15], v[180:183], v[164:167], a[0:15]
	buffer_load_dwordx4 v209, s[4:7], s1 offen lds
	s_mov_b32 m0, s81
	v_mfma_f32_32x32x16_bf16 a[16:31], v[180:183], v[192:195], a[16:31]
	buffer_load_dwordx4 v210, s[4:7], s82 offen lds
	ds_read_b128 a[192:195], v219 offset:0
	s_mov_b32 m0, s83
	v_mfma_f32_32x32x16_bf16 a[32:47], v[184:187], v[164:167], a[32:47]
	buffer_load_dwordx4 v209, s[4:7], s84 offen lds
	ds_read_b128 a[196:199], v220 offset:0
	s_mov_b32 m0, s85
	v_mfma_f32_32x32x16_bf16 a[48:63], v[184:187], v[192:195], a[48:63]
	buffer_load_dwordx4 v210, s[4:7], s86 offen lds
	ds_read_b128 a[200:203], v221 offset:0
	s_mov_b32 m0, s87
	v_mfma_f32_32x32x16_bf16 a[64:79], v[176:179], v[164:167], a[64:79]
	buffer_load_dwordx4 v211, s[20:23], s88 offen lds
	ds_read_b128 a[204:207], v222 offset:0
	s_mov_b32 m0, s89
	v_mfma_f32_32x32x16_bf16 a[80:95], v[176:179], v[192:195], a[80:95]
	buffer_load_dwordx4 v211, s[20:23], s90 offen lds
	ds_read_b128 a[208:211], v219 offset:128
	s_mov_b32 m0, s91
	v_mfma_f32_32x32x16_bf16 a[96:111], v[188:191], v[164:167], a[96:111]
	buffer_load_dwordx4 v211, s[20:23], s92 offen lds
	ds_read_b128 a[212:215], v220 offset:128
	s_mov_b32 m0, s93
	v_mfma_f32_32x32x16_bf16 a[112:127], v[188:191], v[192:195], a[112:127]
	buffer_load_dwordx4 v211, s[20:23], s94 offen lds
	ds_read_b128 a[216:219], v221 offset:128
	v_mfma_f32_32x32x16_bf16 a[0:15], v[172:175], v[128:131], a[0:15]
	ds_read_b128 a[220:223], v222 offset:128
	v_max3_f32 v156, v112, v113, v80
	v_max3_f32 v157, v114, v115, v81
	v_max3_f32 v156, v156, v82, v83
	v_mfma_f32_32x32x16_bf16 a[16:31], v[172:175], v[144:147], a[16:31]
	ds_read_b128 a[224:227], v219 offset:8192
	v_max3_f32 v156, v156, v116, v117
	v_max3_f32 v157, v157, v118, v119
	v_max3_f32 v156, v156, v84, v85
	v_max3_f32 v157, v157, v86, v87
	v_mfma_f32_32x32x16_bf16 a[32:47], v[168:171], v[128:131], a[32:47]
	ds_read_b128 a[228:231], v220 offset:8192
	v_max3_f32 v156, v156, v120, v121
	v_max3_f32 v157, v157, v122, v123
	v_max3_f32 v156, v156, v88, v89
	v_max3_f32 v157, v157, v90, v91
	v_mfma_f32_32x32x16_bf16 a[48:63], v[168:171], v[144:147], a[48:63]
	ds_read_b128 a[232:235], v221 offset:8192
	v_max3_f32 v156, v156, v124, v125
	v_max3_f32 v157, v157, v126, v127
	v_max3_f32 v156, v156, v92, v93
	v_max3_f32 v157, v157, v94, v95
	v_mfma_f32_32x32x16_bf16 a[64:79], v[160:163], v[128:131], a[64:79]
	ds_read_b128 a[236:239], v222 offset:8192
	v_max3_f32 v158, v96, v97, v64
	v_max3_f32 v159, v98, v99, v65
	v_max3_f32 v158, v158, v66, v67
	v_mfma_f32_32x32x16_bf16 a[80:95], v[160:163], v[144:147], a[80:95]
	ds_read_b128 a[240:243], v219 offset:8320
	v_max3_f32 v158, v158, v100, v101
	v_max3_f32 v159, v159, v102, v103
	v_max3_f32 v158, v158, v68, v69
	v_max3_f32 v159, v159, v70, v71
	v_mfma_f32_32x32x16_bf16 a[96:111], v[136:139], v[128:131], a[96:111]
	ds_read_b128 a[244:247], v220 offset:8320
	v_max3_f32 v128, v158, v104, v105
	v_max3_f32 v129, v159, v106, v107
	v_max3_f32 v128, v128, v72, v73
	v_max3_f32 v129, v129, v74, v75
	v_mfma_f32_32x32x16_bf16 a[112:127], v[136:139], v[144:147], a[112:127]
	ds_read_b128 a[248:251], v221 offset:8320
	v_max3_f32 v128, v128, v108, v109
	v_max3_f32 v129, v129, v110, v111
	v_max3_f32 v128, v128, v76, v77
	v_max3_f32 v130, v129, v78, v79
	v_mfma_f32_32x32x16_bf16 a[0:15], v[132:135], v[52:55], a[0:15]
	ds_read_b128 a[252:255], v222 offset:8320
	v_max_f32_e32 v129, v156, v157
	v_max_f32_e32 v128, v128, v130
	v_mov_b32_e32 v131, v129
	v_mov_b32_e32 v130, v128
	v_mfma_f32_32x32x16_bf16 a[16:31], v[132:135], v[140:143], a[16:31]
	v_permlane32_swap_b32_e32 v129, v131
	v_permlane32_swap_b32_e32 v128, v130
	v_max_f32_e32 v129, v129, v131
	v_max_f32_e32 v128, v128, v130
	v_max_f32_e32 v130, v129, v128
	v_mfma_f32_32x32x16_bf16 a[32:47], v[60:63], v[52:55], a[32:47]
	v_cmp_lt_f32_e32 vcc, s79, v130
	s_cmp_lg_u64 vcc, 0
	s_cselect_b64 s[0:1], -1, 0
	s_cbranch_vccnz .LBB2_18

.LBB2_15:
	s_waitcnt lgkmcnt(0)
	v_exp_f32_e32 v80, v80
	v_exp_f32_e32 v81, v81
	v_mfma_f32_32x32x16_bf16 v[112:127], a[192:195], a[128:131], v[16:31]
	ds_read_b64_tr_b16 v[180:181], v208 offset:0
	v_cvt_pk_bf16_f32 v164, v128, v129
	v_exp_f32_e32 v82, v82
	v_exp_f32_e32 v83, v83
	v_mfma_f32_32x32x16_bf16 v[96:111], a[192:195], a[160:163], v[0:15]
	ds_read_b64_tr_b16 v[182:183], v208 offset:0x800
	v_cvt_pk_bf16_f32 v165, v130, v131
	v_mfma_f32_32x32x16_bf16 v[48:63], a[224:227], a[128:131], v[16:31]
	ds_read_b64_tr_b16 v[184:185], v208 offset:0x200
	v_exp_f32_e32 v240, v84
	v_exp_f32_e32 v241, v85
	v_cvt_pk_bf16_f32 v166, v132, v133
	v_mfma_f32_32x32x16_bf16 v[32:47], a[224:227], a[160:163], v[0:15]
	ds_read_b64_tr_b16 v[186:187], v208 offset:0xa00
	ds_read_b64_tr_b16 v[176:177], v208 offset:0x400
	v_exp_f32_e32 v242, v86
	v_exp_f32_e32 v243, v87
	v_cvt_pk_bf16_f32 v167, v134, v135
	v_exp_f32_e32 v198, v88
	v_exp_f32_e32 v199, v89
	v_mfma_f32_32x32x16_bf16 v[112:127], a[196:199], a[132:135], v[112:127]
	ds_read_b64_tr_b16 v[178:179], v208 offset:0xc00
	v_cvt_pk_bf16_f32 v128, v136, v137
	v_exp_f32_e32 v230, v90
	v_exp_f32_e32 v231, v91
	v_mfma_f32_32x32x16_bf16 v[96:111], a[196:199], a[164:167], v[96:111]
	ds_read_b64_tr_b16 v[188:189], v208 offset:0x600
	v_cvt_pk_bf16_f32 v129, v138, v139
	v_exp_f32_e32 v232, v92
	v_exp_f32_e32 v233, v93
	v_mfma_f32_32x32x16_bf16 v[48:63], a[228:231], a[132:135], v[48:63]
	ds_read_b64_tr_b16 v[190:191], v208 offset:0xe00
	v_cvt_pk_bf16_f32 v130, v140, v141
	v_mfma_f32_32x32x16_bf16 v[32:47], a[228:231], a[164:167], v[32:47]
	ds_read_b64_tr_b16 v[172:173], v208 offset:0x1000
	v_exp_f32_e32 v234, v94
	v_exp_f32_e32 v235, v95
	ds_read_b64_tr_b16 v[174:175], v208 offset:0x1800
	v_cvt_pk_bf16_f32 v131, v142, v143
	v_exp_f32_e32 v141, v64
	v_exp_f32_e32 v142, v65
	v_mfma_f32_32x32x16_bf16 v[112:127], a[200:203], a[136:139], v[112:127]
	ds_read_b64_tr_b16 v[168:169], v208 offset:0x1200
	v_cvt_pk_bf16_f32 v192, v144, v145
	v_exp_f32_e32 v143, v66
	v_mfma_f32_32x32x16_bf16 v[96:111], a[200:203], a[168:171], v[96:111]
	ds_read_b64_tr_b16 v[170:171], v208 offset:0x1a00
	v_exp_f32_e32 v244, v67
	v_cvt_pk_bf16_f32 v193, v146, v147
	v_mfma_f32_32x32x16_bf16 v[48:63], a[232:235], a[136:139], v[48:63]
	ds_read_b64_tr_b16 v[160:161], v208 offset:0x1400
	v_exp_f32_e32 v245, v68
	v_exp_f32_e32 v246, v69
	v_cvt_pk_bf16_f32 v194, v148, v149
	v_mfma_f32_32x32x16_bf16 v[32:47], a[232:235], a[168:171], v[32:47]
	ds_read_b64_tr_b16 v[162:163], v208 offset:0x1c00
	ds_read_b64_tr_b16 v[136:137], v208 offset:0x1600
	v_exp_f32_e32 v247, v70
	v_exp_f32_e32 v248, v71
	v_cvt_pk_bf16_f32 v195, v150, v151
	v_exp_f32_e32 v148, v72
	v_exp_f32_e32 v149, v73
	v_mfma_f32_32x32x16_bf16 v[112:127], a[204:207], a[140:143], v[112:127]
	ds_read_b64_tr_b16 v[138:139], v208 offset:0x1e00
	v_cvt_pk_bf16_f32 v144, v152, v153
	v_exp_f32_e32 v150, v74
	v_exp_f32_e32 v151, v75
	v_mfma_f32_32x32x16_bf16 v[96:111], a[204:207], a[172:175], v[96:111]
	ds_read_b64_tr_b16 v[132:133], v208 offset:0x2000
	v_cvt_pk_bf16_f32 v145, v154, v155
	v_exp_f32_e32 v152, v76
	v_exp_f32_e32 v153, v77
	v_mfma_f32_32x32x16_bf16 v[48:63], a[236:239], a[140:143], v[48:63]
	ds_read_b64_tr_b16 v[134:135], v208 offset:0x2800
	v_cvt_pk_bf16_f32 v146, v156, v157
	v_mfma_f32_32x32x16_bf16 v[32:47], a[236:239], a[172:175], v[32:47]
	ds_read_b64_tr_b16 v[92:93], v208 offset:0x2200
	v_exp_f32_e32 v154, v78
	v_exp_f32_e32 v155, v79
	ds_read_b64_tr_b16 v[94:95], v208 offset:0x2a00
	v_cvt_pk_bf16_f32 v147, v158, v159
	s_mov_b32 s0, s51
	v_mfma_f32_32x32x16_bf16 v[112:127], a[208:211], a[144:147], v[112:127]
	ds_read_b64_tr_b16 v[88:89], v208 offset:0x2400
	v_cvt_pk_bf16_f32 v84, v80, v81
	v_add_f32_e32 v64, v237, v80
	v_add_f32_e32 v65, v236, v81
	s_add_i32 s1, s17, 0xffffa000
	v_mfma_f32_32x32x16_bf16 v[96:111], a[208:211], a[176:179], v[96:111]
	ds_read_b64_tr_b16 v[90:91], v208 offset:0x2c00
	v_cvt_pk_bf16_f32 v85, v82, v83
	v_add_f32_e32 v64, v64, v82
	v_add_f32_e32 v65, v65, v83
	s_mov_b32 s81, s53
	v_mfma_f32_32x32x16_bf16 v[48:63], a[240:243], a[144:147], v[48:63]
	ds_read_b64_tr_b16 v[80:81], v208 offset:0x2600
	v_cvt_pk_bf16_f32 v86, v240, v241
	v_add_f32_e32 v64, v64, v240
	v_add_f32_e32 v65, v65, v241
	s_add_i32 s82, s17, 0xffffc000
	v_mfma_f32_32x32x16_bf16 v[32:47], a[240:243], a[176:179], v[32:47]
	ds_read_b64_tr_b16 v[82:83], v208 offset:0x2e00
	ds_read_b64_tr_b16 v[76:77], v208 offset:0x3000
	v_cvt_pk_bf16_f32 v87, v242, v243
	v_add_f32_e32 v64, v64, v242
	v_add_f32_e32 v65, v65, v243
	s_mov_b32 s83, s55
	v_mfma_f32_32x32x16_bf16 v[112:127], a[212:215], a[148:151], v[112:127]
	ds_read_b64_tr_b16 v[78:79], v208 offset:0x3800
	v_add_f32_e32 v64, v64, v198
	v_add_f32_e32 v65, v65, v199
	s_add_i32 s84, s17, 0xffffe000
	v_mfma_f32_32x32x16_bf16 v[96:111], a[212:215], a[180:183], v[96:111]
	ds_read_b64_tr_b16 v[72:73], v208 offset:0x3200
	v_add_f32_e32 v64, v64, v230
	v_add_f32_e32 v65, v65, v231
	s_mov_b32 s85, s57
	v_mfma_f32_32x32x16_bf16 v[48:63], a[244:247], a[148:151], v[48:63]
	ds_read_b64_tr_b16 v[74:75], v208 offset:0x3a00
	v_add_f32_e32 v64, v64, v232
	v_add_f32_e32 v65, v65, v233
	s_mov_b32 s86, s17
	v_mfma_f32_32x32x16_bf16 v[32:47], a[244:247], a[180:183], v[32:47]
	ds_read_b64_tr_b16 v[68:69], v208 offset:0x3400
	ds_read_b64_tr_b16 v[70:71], v208 offset:0x3c00
	v_add_f32_e32 v156, v64, v234
	v_add_f32_e32 v157, v65, v235
	s_mov_b32 s87, s31
	v_mfma_f32_32x32x16_bf16 v[112:127], a[216:219], a[152:155], v[112:127]
	ds_read_b64_tr_b16 v[64:65], v208 offset:0x3600
	v_cvt_pk_bf16_f32 v140, v141, v142
	v_add_f32_e32 v158, v238, v141
	v_add_f32_e32 v142, v239, v142
	v_mfma_f32_32x32x16_bf16 v[96:111], a[216:219], a[184:187], v[96:111]
	ds_read_b64_tr_b16 v[66:67], v208 offset:0x3e00
	v_cvt_pk_bf16_f32 v141, v143, v244
	v_add_f32_e32 v143, v158, v143
	v_add_f32_e32 v158, v142, v244
	v_mfma_f32_32x32x16_bf16 v[48:63], a[248:251], a[152:155], v[48:63]
	s_mov_b32 s88, s59
	v_cvt_pk_bf16_f32 v142, v245, v246
	v_add_f32_e32 v159, v143, v245
	v_add_f32_e32 v158, v158, v246
	v_mfma_f32_32x32x16_bf16 v[32:47], a[248:251], a[184:187], v[32:47]
	s_add_i32 s89, s17, 0xfffda080
	v_cvt_pk_bf16_f32 v143, v247, v248
	v_add_f32_e32 v159, v159, v247
	v_add_f32_e32 v158, v158, v248
	v_mfma_f32_32x32x16_bf16 v[112:127], a[220:223], a[156:159], v[112:127]
	s_mov_b32 s90, s61
	v_add_f32_e32 v159, v159, v148
	v_add_f32_e32 v158, v158, v149
	v_mfma_f32_32x32x16_bf16 v[96:111], a[220:223], a[188:191], v[96:111]
	v_add_f32_e32 v159, v159, v150
	v_add_f32_e32 v158, v158, v151
	v_mfma_f32_32x32x16_bf16 v[48:63], a[252:255], a[156:159], v[48:63]
	s_mov_b32 s91, s62
	v_add_f32_e32 v159, v159, v152
	v_add_f32_e32 v158, v158, v153
	v_mfma_f32_32x32x16_bf16 v[32:47], a[252:255], a[188:191], v[32:47]
	s_add_i32 s92, s17, 0xfffde080
	v_add_f32_e32 v159, v159, v154
	v_add_f32_e32 v158, v158, v155
	v_add_f32_e32 v156, v156, v157
	s_waitcnt vmcnt(0) lgkmcnt(0)
	s_barrier
	v_add_f32_e32 v158, v159, v158
	v_mov_b32_e32 v157, v156
	v_mov_b32_e32 v159, v158
	s_nop 0
	v_permlane32_swap_b32_e32 v156, v157
	v_permlane32_swap_b32_e32 v158, v159
	v_add_f32_e32 v156, v156, v157
	v_add_f32_e32 v158, v158, v159
	v_add_f32_e32 v197, v197, v156
	v_add_f32_e32 v196, v196, v158
	s_mov_b32 m0, s0
	v_mfma_f32_32x32x16_bf16 a[0:15], v[180:183], v[164:167], a[0:15]
	buffer_load_dwordx4 v209, s[4:7], s1 offen lds
	s_mov_b32 m0, s81
	v_mfma_f32_32x32x16_bf16 a[16:31], v[180:183], v[192:195], a[16:31]
	buffer_load_dwordx4 v210, s[4:7], s82 offen lds
	ds_read_b128 a[192:195], v204 offset:0
	s_mov_b32 m0, s83
	v_mfma_f32_32x32x16_bf16 a[32:47], v[184:187], v[164:167], a[32:47]
	buffer_load_dwordx4 v209, s[4:7], s84 offen lds
	ds_read_b128 a[196:199], v205 offset:0
	s_mov_b32 m0, s85
	v_mfma_f32_32x32x16_bf16 a[48:63], v[184:187], v[192:195], a[48:63]
	buffer_load_dwordx4 v210, s[4:7], s86 offen lds
	ds_read_b128 a[200:203], v206 offset:0
	s_mov_b32 m0, s87
	v_mfma_f32_32x32x16_bf16 a[64:79], v[176:179], v[164:167], a[64:79]
	buffer_load_dwordx4 v211, s[20:23], s19 offen lds
	ds_read_b128 a[204:207], v207 offset:0
	s_mov_b32 m0, s88
	v_mfma_f32_32x32x16_bf16 a[80:95], v[176:179], v[192:195], a[80:95]
	buffer_load_dwordx4 v211, s[20:23], s89 offen lds
	ds_read_b128 a[208:211], v204 offset:128
	s_mov_b32 m0, s90
	v_mfma_f32_32x32x16_bf16 a[96:111], v[188:191], v[164:167], a[96:111]
	buffer_load_dwordx4 v211, s[20:23], s24 offen lds
	ds_read_b128 a[212:215], v205 offset:128
	s_mov_b32 m0, s91
	v_mfma_f32_32x32x16_bf16 a[112:127], v[188:191], v[192:195], a[112:127]
	buffer_load_dwordx4 v211, s[20:23], s92 offen lds
	ds_read_b128 a[216:219], v206 offset:128
	v_mfma_f32_32x32x16_bf16 a[0:15], v[172:175], v[128:131], a[0:15]
	ds_read_b128 a[220:223], v207 offset:128
	v_max3_f32 v156, v112, v113, v48
	v_max3_f32 v157, v114, v115, v49
	v_max3_f32 v156, v156, v50, v51
	v_mfma_f32_32x32x16_bf16 a[16:31], v[172:175], v[144:147], a[16:31]
	ds_read_b128 a[224:227], v204 offset:8192
	v_max3_f32 v156, v156, v116, v117
	v_max3_f32 v157, v157, v118, v119
	v_max3_f32 v156, v156, v52, v53
	v_max3_f32 v157, v157, v54, v55
	v_mfma_f32_32x32x16_bf16 a[32:47], v[168:171], v[128:131], a[32:47]
	ds_read_b128 a[228:231], v205 offset:8192
	v_max3_f32 v156, v156, v120, v121
	v_max3_f32 v157, v157, v122, v123
	v_max3_f32 v156, v156, v56, v57
	v_max3_f32 v157, v157, v58, v59
	v_mfma_f32_32x32x16_bf16 a[48:63], v[168:171], v[144:147], a[48:63]
	ds_read_b128 a[232:235], v206 offset:8192
	v_max3_f32 v156, v156, v124, v125
	v_max3_f32 v157, v157, v126, v127
	v_max3_f32 v156, v156, v60, v61
	v_max3_f32 v157, v157, v62, v63
	v_mfma_f32_32x32x16_bf16 a[64:79], v[160:163], v[128:131], a[64:79]
	ds_read_b128 a[236:239], v207 offset:8192
	v_max3_f32 v158, v96, v97, v32
	v_max3_f32 v159, v98, v99, v33
	v_max3_f32 v158, v158, v34, v35
	v_mfma_f32_32x32x16_bf16 a[80:95], v[160:163], v[144:147], a[80:95]
	ds_read_b128 a[240:243], v204 offset:8320
	v_max3_f32 v158, v158, v100, v101
	v_max3_f32 v159, v159, v102, v103
	v_max3_f32 v158, v158, v36, v37
	v_max3_f32 v159, v159, v38, v39
	v_mfma_f32_32x32x16_bf16 a[96:111], v[136:139], v[128:131], a[96:111]
	ds_read_b128 a[244:247], v205 offset:8320
	v_max3_f32 v128, v158, v104, v105
	v_max3_f32 v129, v159, v106, v107
	v_max3_f32 v128, v128, v40, v41
	v_max3_f32 v129, v129, v42, v43
	v_mfma_f32_32x32x16_bf16 a[112:127], v[136:139], v[144:147], a[112:127]
	ds_read_b128 a[248:251], v206 offset:8320
	v_max3_f32 v128, v128, v108, v109
	v_max3_f32 v129, v129, v110, v111
	v_max3_f32 v128, v128, v44, v45
	v_max3_f32 v130, v129, v46, v47
	v_mfma_f32_32x32x16_bf16 a[0:15], v[132:135], v[84:87], a[0:15]
	ds_read_b128 a[252:255], v207 offset:8320
	v_max_f32_e32 v129, v156, v157
	v_max_f32_e32 v128, v128, v130
	v_mov_b32_e32 v131, v129
	v_mov_b32_e32 v130, v128
	v_mfma_f32_32x32x16_bf16 a[16:31], v[132:135], v[140:143], a[16:31]
	v_permlane32_swap_b32_e32 v129, v131
	v_permlane32_swap_b32_e32 v128, v130
	v_max_f32_e32 v129, v129, v131
	v_max_f32_e32 v128, v128, v130
	v_max_f32_e32 v130, v129, v128
	v_mfma_f32_32x32x16_bf16 a[32:47], v[92:95], v[84:87], a[32:47]
	v_cmp_lt_f32_e32 vcc, s79, v130
	s_cmp_lg_u64 vcc, 0
	s_cselect_b64 s[0:1], -1, 0
	s_cbranch_vccnz .LBB2_20
